# v32
# speedup vs baseline: 1.0127x; 1.0020x over previous
.Lp1_noinit:
	s_or_b64 exec, exec, s[26:27]
	s_cmp_lt_u32 s31, 4
	s_cbranch_scc1 .Lp1_nostagger
	s_sleep 100
.Lp1_nostagger:
.LBB0_9:
	s_waitcnt vmcnt(15)
	v_cvt_pk_bf16_f32 v2, v34, v35
	v_cvt_pk_bf16_f32 v3, v36, v37
	s_waitcnt vmcnt(11)
	v_cvt_pk_bf16_f32 v10, v50, v51
	v_cvt_pk_bf16_f32 v11, v52, v53
	v_cvt_pk_bf16_f32 v4, v38, v39
	v_cvt_pk_bf16_f32 v5, v40, v41
	ds_write2_b64 v212, v[2:3], v[10:11] offset1:68
	s_waitcnt vmcnt(10)
	v_cvt_pk_bf16_f32 v2, v54, v55
	v_cvt_pk_bf16_f32 v3, v56, v57
	v_cvt_pk_bf16_f32 v6, v42, v43
	v_cvt_pk_bf16_f32 v7, v44, v45
	ds_write2_b64 v215, v[4:5], v[2:3] offset0:16 offset1:84
	s_waitcnt vmcnt(9)
	v_cvt_pk_bf16_f32 v2, v58, v59
	v_cvt_pk_bf16_f32 v3, v60, v61
	v_cvt_pk_bf16_f32 v8, v46, v47
	v_cvt_pk_bf16_f32 v9, v48, v49
	ds_write2_b64 v216, v[6:7], v[2:3] offset0:32 offset1:100
	s_waitcnt vmcnt(8)
	v_cvt_pk_bf16_f32 v2, v62, v63
	v_cvt_pk_bf16_f32 v3, v64, v65
	ds_write2_b64 v217, v[8:9], v[2:3] offset0:48 offset1:116
	s_waitcnt vmcnt(7)
	v_cvt_pk_bf16_f32 v2, v66, v67
	v_cvt_pk_bf16_f32 v3, v68, v69
	s_waitcnt vmcnt(3)
	v_cvt_pk_bf16_f32 v10, v82, v83
	v_cvt_pk_bf16_f32 v11, v84, v85
	v_cvt_pk_bf16_f32 v4, v70, v71
	v_cvt_pk_bf16_f32 v5, v72, v73
	ds_write2_b64 v212, v[2:3], v[10:11] offset0:136 offset1:204
	s_waitcnt vmcnt(2)
	v_cvt_pk_bf16_f32 v2, v86, v87
	v_cvt_pk_bf16_f32 v3, v88, v89
	v_cvt_pk_bf16_f32 v6, v74, v75
	v_cvt_pk_bf16_f32 v7, v76, v77
	ds_write2_b64 v215, v[4:5], v[2:3] offset0:152 offset1:220
	s_waitcnt vmcnt(1)
	v_cvt_pk_bf16_f32 v2, v90, v91
	v_cvt_pk_bf16_f32 v3, v92, v93
	v_cvt_pk_bf16_f32 v8, v78, v79
	v_cvt_pk_bf16_f32 v9, v80, v81
	ds_write2_b64 v216, v[6:7], v[2:3] offset0:168 offset1:236
	s_waitcnt vmcnt(0)
	v_cvt_pk_bf16_f32 v2, v94, v95
	v_cvt_pk_bf16_f32 v3, v96, v97
	ds_write2_b64 v217, v[8:9], v[2:3] offset0:184 offset1:252
	s_add_i32 s26, s35, 8
	s_cmpk_lt_i32 s26, 0x80
	s_mov_b64 s[24:25], -1
	s_cbranch_scc1 .LBB0_15
	global_load_dwordx4 v[26:29], v[134:135], off offset:16
	global_load_dwordx4 v[30:33], v[134:135], off
	global_load_dwordx4 v[18:21], v[134:135], off offset:144
	global_load_dwordx4 v[22:25], v[134:135], off offset:128
	global_load_dwordx4 v[10:13], v[134:135], off offset:272
	global_load_dwordx4 v[14:17], v[134:135], off offset:256
	global_load_dwordx4 v[2:5], v[134:135], off offset:400
	global_load_dwordx4 v[6:9], v[134:135], off offset:384
	s_mov_b64 s[24:25], 0
